# also skip padded 64-row MFMA clusters in the expert-down main GEMM
# baseline (speedup 1.0000x reference)
; #define PG8_STAGE(bufoff, gbase, voff) do { _Pragma("unroll") for (int _i = 0; _i < 2; ++_i) \
;         __builtin_amdgcn_global_load_lds((const unsigned*)((const char*)(gbase) + (voff)[_i]), (LAS unsigned*)(lds + (bufoff) + ldsw + _i * 8192), 16, 0, 0); } while (0)
; #define PG8_WAIT_V(n) asm volatile("s_waitcnt vmcnt(" #n ")" ::: "memory")
; #define PG8_BAR __builtin_amdgcn_s_barrier()
;     ...
;     Unit cur, nxt; int ui = 0;
;     if (!S.next(0, cur)) return;
;     f32x4 acc[2][2][4][2];
; #pragma unroll
;     for (int a = 0; a < 2; ++a)
; #pragma unroll
;         for (int b = 0; b < 2; ++b)
; #pragma unroll
;             for (int m = 0; m < 4; ++m)
; #pragma unroll
;                 for (int n = 0; n < 2; ++n) acc[a][b][m][n] = (f32x4){0.f, 0.f, 0.f, 0.f};
;     i32x8 At[4], B0[2], B1[2];
;     const char* cA = cur.A; const char* cB = cur.B;
;     if constexpr (SP2) {
;         PG8_STAGE(PG8_SB(0, 0), cB, voffB); PG8_STAGE(PG8_SB(0, 1), cB + hstep, voffB); PG8_STAGE(PG8_SA(0, 0), cA, voffA); PG8_STAGE(PG8_SA(0, 1), cA + hstep, voffA);
;         if (wr == 1) PG8_BAR;
;         PG8_WAIT_V(2); PG8_BAR;
;         PG8_STAGE(PG8_SB(1, 0), cB + kstep, voffB); PG8_STAGE(PG8_SA(1, 0), cA + kstep, voffA); PG8_STAGE(PG8_SB(1, 1), cB + hstep + kstep, voffB);
;         PG8_WAIT_V(6); PG8_BAR;
;     __device__ __forceinline__ bool next(int i, pg8::Unit& u) const {
;         const int Lx = i * G + c; if (Lx >= 512) return false;
;         pg8::tile_of(Lx, 64, 8, u.pm, u.pn); const int e = tiles[1 + u.pm]; u.z = 0;
;         u.A = A0 + (size_t)u.pm * tsA; u.B = B0 + (size_t)e * estride + (size_t)u.pn * tsB; return true;
;     }
.LBB0_2322:
	s_ashr_i32 s21, s21, 3
	s_add_i32 s21, s24, s21
	s_ashr_i32 s24, s21, 31
	s_lshr_b32 s24, s24, 26
	s_add_i32 s24, s21, s24
	s_ashr_i32 s25, s24, 6
	s_andn2_b32 s24, s24, 63
	s_sub_i32 s21, s21, s24
	s_bfe_i32 s24, s21, 0x80000
	s_bfe_u32 s24, s24, 0x3000c
	s_add_i32 s24, s21, s24
	s_bfe_i32 s28, s24, 0x80000
	s_and_b32 s24, s24, 0xf8
	s_sub_i32 s21, s21, s24
	s_lshl_b32 s25, s25, 3
	s_sext_i32_i8 s21, s21
	s_add_i32 s66, s25, s21
	v_mad_u64_u32 v[164:165], s[22:23], s0, v198, v[162:163]
	s_lshr_b32 s5, s36, 6
	s_ashr_i32 s1, s0, 31
	s_sext_i32_i16 s28, s28
	s_ashr_i32 s67, s66, 31
	s_lshr_b32 s4, s36, 8
	s_lshl_b64 s[22:23], s[0:1], 7
	s_lshl_b32 s3, s5, 10
	s_lshr_b32 s37, s28, 3
	s_lshl_b64 s[24:25], s[66:67], 2
	s_add_u32 s24, s10, s24
	s_addc_u32 s25, s11, s25
	v_mov_b32_e32 v165, 0
	global_load_dword v2, v165, s[24:25] offset:4
	v_lshrrev_b32_e32 v254, 8, v0
	v_lshlrev_b32_e32 v254, 6, v254
	v_lshl_add_u32 v254, s66, 8, v254
	v_lshlrev_b32_e32 v254, 2, v254
	v_add_u32_e32 v254, 0x570000, v254
	global_load_dword v255, v254, s[52:53] offset:512
	global_load_dword v254, v254, s[52:53]
	v_mad_u64_u32 v[166:167], s[24:25], s0, v197, v[162:163]
	v_mad_u64_u32 v[168:169], s[24:25], s0, v199, v[162:163]
	v_mad_u64_u32 v[170:171], s[24:25], s0, v200, v[162:163]
	s_mul_i32 s24, s66, 0x1c0000
	s_mul_hi_i32 s21, s66, 0x1c0000
	s_add_u32 s68, s12, s24
	s_addc_u32 s69, s13, s21
	v_mov_b32_e32 v171, v165
	v_mov_b32_e32 v167, v165
	v_mov_b32_e32 v169, v165
	s_mov_b32 s45, 0
	v_lshl_add_u64 v[8:9], s[68:69], 0, v[166:167]
	v_lshl_add_u64 v[12:13], s[68:69], 0, v[168:169]
	s_waitcnt vmcnt(0)
	v_readfirstlane_b32 s21, v2
	s_mul_hi_i32 s24, s21, 0x1c00000
	s_mul_i32 s21, s21, 0x1c00000
	s_add_u32 s21, s18, s21
	s_addc_u32 s24, s19, s24
	s_ashr_i32 s25, s28, 3
	s_mul_hi_i32 s28, s25, 0x1c0000
	s_mul_i32 s25, s25, 0x1c0000
	s_add_u32 s70, s21, s25
	s_addc_u32 s71, s24, s28
	s_add_i32 s21, s3, 0
	s_add_i32 m0, s21, 0x10000
	v_lshl_add_u64 v[10:11], s[70:71], 0, v[164:165]
	global_load_lds_dwordx4 v164, s[70:71]
	s_add_i32 m0, s21, 0x12000
	s_add_u32 s24, s70, s22
	global_load_lds_dwordx4 v170, s[70:71]
	s_addc_u32 s25, s71, s23
	s_add_i32 m0, s21, 0x14000
	s_add_i32 s34, s21, 0x2000
	global_load_lds_dwordx4 v164, s[24:25]
	s_add_i32 m0, s21, 0x16000
	s_add_u32 s28, s68, s22
	global_load_lds_dwordx4 v170, s[24:25]
	s_mov_b32 m0, s21
	s_addc_u32 s29, s69, s23
	global_load_lds_dwordx4 v166, s[68:69]
	s_add_i32 s35, s21, 0x4000
	s_mov_b32 m0, s34
	s_add_i32 s44, s21, 0x6000
	global_load_lds_dwordx4 v168, s[68:69]
	s_mov_b32 m0, s35
	s_cmp_eq_u32 s4, 1
	global_load_lds_dwordx4 v166, s[28:29]
	s_mov_b32 m0, s44
	v_lshl_add_u64 v[6:7], s[70:71], 0, v[170:171]
	global_load_lds_dwordx4 v168, s[28:29]
	v_lshl_add_u64 v[4:5], s[24:25], 0, v[164:165]
	v_lshl_add_u64 v[2:3], s[24:25], 0, v[170:171]
	s_cselect_b64 s[24:25], -1, 0
	s_cmp_lg_u32 s4, 1
	s_cbranch_scc1 .LBB0_2324
	s_barrier

;     ...
;     for (;;) {
;         const bool has_next = S.next(ui + 1, nxt);
;         const char* nA = has_next ? nxt.A : cA; const char* nB = has_next ? nxt.B : cB;
;     __device__ __forceinline__ bool next(int i, pg8::Unit& u) const {
;         const int Lx = i * G + c; if (Lx >= 512) return false;
.LBB0_2327:
	v_mov_b32_e32 v252, v254
	v_mov_b32_e32 v253, v255
	s_add_i32 s45, s45, 1
	s_mul_i32 s61, s45, s33
	s_add_i32 s61, s61, s2
	s_cmpk_lt_i32 s61, 0x200
	s_cselect_b64 s[4:5], -1, 0
	s_cmpk_gt_i32 s61, 0x1ff
	s_cbranch_scc1 .LBB0_2333
	s_ashr_i32 s60, s61, 31
	s_lshr_b32 s60, s60, 29
	s_add_i32 s62, s61, s60
	s_and_b32 s60, s62, -8
	s_sub_i32 s63, s61, s60
	s_cmp_gt_i32 s63, -1
	s_mov_b64 s[60:61], -1
	s_cbranch_scc0 .LBB0_2330
	s_lshl_b32 s64, s63, 6
	s_mov_b64 s[60:61], 0

;     __device__ __forceinline__ bool next(int i, pg8::Unit& u) const {
;     ...
;         pg8::tile_of(Lx, 64, 8, u.pm, u.pn); const int e = tiles[1 + u.pm]; u.z = 0;
;         u.A = A0 + (size_t)u.pm * tsA; u.B = B0 + (size_t)e * estride + (size_t)u.pn * tsB; return true;
;     }
.LBB0_2332:
	s_ashr_i32 s60, s62, 3
	s_add_i32 s60, s64, s60
	s_ashr_i32 s61, s60, 31
	s_lshr_b32 s61, s61, 26
	s_add_i32 s61, s60, s61
	s_ashr_i32 s62, s61, 6
	s_and_b32 s61, s61, 0xffc0
	s_sub_i32 s60, s60, s61
	s_bfe_i32 s61, s60, 0x80000
	s_bfe_u32 s61, s61, 0x3000c
	s_add_i32 s61, s60, s61
	s_bfe_i32 s63, s61, 0x80000
	s_and_b32 s61, s61, 0xf8
	s_sub_i32 s60, s60, s61
	s_lshl_b32 s62, s62, 3
	s_sext_i32_i8 s60, s60
	s_add_i32 s60, s62, s60
	s_sext_i32_i16 s63, s63
	s_ashr_i32 s61, s60, 31
	s_ashr_i32 s78, s63, 3
	s_lshl_b64 s[62:63], s[60:61], 2
	s_add_u32 s62, s10, s62
	s_addc_u32 s63, s11, s63
	global_load_dword v2, v165, s[62:63] offset:4
	v_lshrrev_b32_e32 v254, 8, v0
	v_lshlrev_b32_e32 v254, 6, v254
	v_lshl_add_u32 v254, s60, 8, v254
	v_lshlrev_b32_e32 v254, 2, v254
	v_add_u32_e32 v254, 0x570000, v254
	global_load_dword v255, v254, s[52:53] offset:512
	global_load_dword v254, v254, s[52:53]
	s_mul_i32 s62, s60, 0x1c0000
	s_mul_hi_i32 s63, s60, 0x1c0000
	s_add_u32 s62, s12, s62
	s_addc_u32 s63, s13, s63
	s_mul_i32 s72, s78, 0x1c0000
	s_mul_hi_i32 s61, s78, 0x1c0000
	s_waitcnt vmcnt(0)
	v_readfirstlane_b32 s64, v2
	s_mul_hi_i32 s65, s64, 0x1c00000
	s_mul_i32 s64, s64, 0x1c00000
	s_add_u32 s64, s18, s64
	s_addc_u32 s65, s19, s65
	s_add_u32 s64, s64, s72
	s_addc_u32 s65, s65, s61

; #define PG8_STAGE(bufoff, gbase, voff) do { _Pragma("unroll") for (int _i = 0; _i < 2; ++_i) \
;         __builtin_amdgcn_global_load_lds((const unsigned*)((const char*)(gbase) + (voff)[_i]), (LAS unsigned*)(lds + (bufoff) + ldsw + _i * 8192), 16, 0, 0); } while (0)
; #define PG8_LDA(dst, b, h) do { _Pragma("unroll") for (int m = 0; m < 4; ++m) dst[m] = PG8_LD8(lds + PG8_SA(b, h) + aoff + m * 2048); } while (0)
; #define PG8_LDB(dst, b, h) do { _Pragma("unroll") for (int n = 0; n < 2; ++n) dst[n] = PG8_LD8(lds + PG8_SB(b, h) + boff + n * 2048); } while (0)
; #define PG8_WAIT_V(n) asm volatile("s_waitcnt vmcnt(" #n ")" ::: "memory")
; #define PG8_WAIT_L(n) asm volatile("s_waitcnt lgkmcnt(" #n ")" ::: "memory")
; #define PG8_BAR __builtin_amdgcn_s_barrier()
; #define PG8_SCHED __builtin_amdgcn_sched_barrier(0)
;     ...
;         for (int t = 0; t < nt; t += 2) {
;             const bool last = (t == nt - 2);
;             const char* a1 = cA + (size_t)(t + 1) * kstep;
;             const char* a2 = last ? nA : cA + (size_t)(t + 2) * kstep; const char* b2 = last ? nB : cB + (size_t)(t + 2) * kstep;
;             const char* a3 = a2 + kstep; const char* b3 = b2 + kstep;
;             if constexpr (SP2) {
;             PG8_LDB(B0, 0, 0); PG8_LDB(B1, 0, 1); PG8_SCHED; PG8_LDA(At, 0, 0); PG8_STAGE(PG8_SA(1, 1), a1 + hstep, voffA);
;             PG8_WAIT_V(8); PG8_WAIT_L(0); PG8_BAR; PG8_MMA(0, 0, At, B0); PG8_MMA(0, 1, At, B1); PG8_BAR; PG8_SCHED;
;             PG8_LDA(At, 0, 1); PG8_STAGE(PG8_SB(0, 0), b2, voffB); PG8_STAGE(PG8_SB(0, 1), b2 + hstep, voffB); PG8_STAGE(PG8_SA(0, 0), a2, voffA);
;             PG8_WAIT_V(8); PG8_WAIT_L(0); PG8_BAR; PG8_MMA(1, 0, At, B0); PG8_MMA(1, 1, At, B1); PG8_BAR; PG8_SCHED;
.LBB0_2335:
	ds_read_b128 v[18:21], v203
	ds_read_b128 v[22:25], v203 offset:1024
	ds_read_b128 v[26:29], v203 offset:2048
	ds_read_b128 v[30:33], v203 offset:3072
	ds_read_b128 v[2:5], v204
	ds_read_b128 v[6:9], v204 offset:1024
	ds_read_b128 v[10:13], v204 offset:2048
	ds_read_b128 v[14:17], v204 offset:3072
	s_add_i32 s81, s70, 2
	s_add_u32 s72, s68, 0x80
	s_addc_u32 s71, s69, 0
	s_cmp_eq_u32 s57, s70
	s_cselect_b32 s70, s62, s72
	s_cselect_b32 s71, s63, s71
	s_cselect_b32 s73, s65, s80
	s_cselect_b32 s72, s64, s61
	v_lshl_add_u64 v[184:185], s[68:69], 0, v[172:173]
	s_add_i32 m0, s21, 0xc000
	ds_read_b128 v[176:179], v205
	ds_read_b128 v[180:183], v205 offset:1024
	ds_read_b128 v[206:209], v205 offset:2048
	ds_read_b128 v[210:213], v205 offset:3072
	ds_read_b128 v[214:217], v205 offset:4096
	ds_read_b128 v[218:221], v205 offset:5120
	ds_read_b128 v[222:225], v205 offset:6144
	ds_read_b128 v[226:229], v205 offset:7168
	global_load_lds_dwordx4 v[184:185], off
	v_lshl_add_u64 v[184:185], s[68:69], 0, v[174:175]
	s_add_i32 m0, s21, 0xe000
	s_nop 0
	global_load_lds_dwordx4 v[184:185], off
	s_waitcnt vmcnt(8)
	s_waitcnt lgkmcnt(0)
	s_barrier
	v_cmp_eq_f32_e32 vcc, 0, v252
	s_cbranch_vccnz .Lp22sk_0
	s_setprio 1
	s_waitcnt lgkmcnt(0)
	v_mfma_f32_16x16x128_f8f6f4 v[158:161], v[18:25], v[176:183], v[158:161]
	v_mfma_f32_16x16x128_f8f6f4 v[154:157], v[26:33], v[176:183], v[154:157]
	v_mfma_f32_16x16x128_f8f6f4 v[142:145], v[18:25], v[206:213], v[142:145]
	v_mfma_f32_16x16x128_f8f6f4 v[138:141], v[26:33], v[206:213], v[138:141]
	v_mfma_f32_16x16x128_f8f6f4 v[126:129], v[18:25], v[214:221], v[126:129]
	v_mfma_f32_16x16x128_f8f6f4 v[122:125], v[26:33], v[214:221], v[122:125]
	v_mfma_f32_16x16x128_f8f6f4 v[110:113], v[18:25], v[222:229], v[110:113]
	v_mfma_f32_16x16x128_f8f6f4 v[106:109], v[26:33], v[222:229], v[106:109]
	s_nop 7
	s_setprio 0
	s_setprio 1
	v_mfma_f32_16x16x128_f8f6f4 v[150:153], v[2:9], v[176:183], v[150:153]
	v_mfma_f32_16x16x128_f8f6f4 v[146:149], v[10:17], v[176:183], v[146:149]
	v_mfma_f32_16x16x128_f8f6f4 v[134:137], v[2:9], v[206:213], v[134:137]
	v_mfma_f32_16x16x128_f8f6f4 v[130:133], v[10:17], v[206:213], v[130:133]
	v_mfma_f32_16x16x128_f8f6f4 v[118:121], v[2:9], v[214:221], v[118:121]
	v_mfma_f32_16x16x128_f8f6f4 v[114:117], v[10:17], v[214:221], v[114:117]
	v_mfma_f32_16x16x128_f8f6f4 v[102:105], v[2:9], v[222:229], v[102:105]
	v_mfma_f32_16x16x128_f8f6f4 v[98:101], v[10:17], v[222:229], v[98:101]
	s_nop 7
	s_setprio 0
.Lp22sk_0:
	s_barrier
	s_add_i32 s82, s59, s3
	v_lshl_add_u64 v[176:177], s[72:73], 0, v[164:165]
	s_mov_b32 m0, s82
	ds_read_b128 v[206:209], v205 offset:16384
	ds_read_b128 v[210:213], v205 offset:17408
	ds_read_b128 v[214:217], v205 offset:18432
	ds_read_b128 v[218:221], v205 offset:19456
	ds_read_b128 v[222:225], v205 offset:20480
	ds_read_b128 v[226:229], v205 offset:21504
	ds_read_b128 v[230:233], v205 offset:22528
	ds_read_b128 v[234:237], v205 offset:23552
	global_load_lds_dwordx4 v[176:177], off
	s_add_i32 m0, s82, 0x2000
	v_lshl_add_u64 v[178:179], s[72:73], 0, v[170:171]
	s_add_u32 s72, s72, s22
	s_addc_u32 s73, s73, s23
	s_add_i32 s82, s67, s3
	global_load_lds_dwordx4 v[178:179], off
	v_lshl_add_u64 v[180:181], s[72:73], 0, v[164:165]
	s_mov_b32 m0, s82
	v_lshl_add_u64 v[182:183], s[72:73], 0, v[170:171]
	global_load_lds_dwordx4 v[180:181], off
	s_add_i32 m0, s82, 0x2000
	v_lshl_add_u64 v[184:185], s[70:71], 0, v[166:167]
	global_load_lds_dwordx4 v[182:183], off
	s_mov_b32 m0, s21
	v_lshl_add_u64 v[186:187], s[70:71], 0, v[168:169]
	global_load_lds_dwordx4 v[184:185], off
	s_mov_b32 m0, s34
	s_nop 0
	global_load_lds_dwordx4 v[186:187], off
	s_waitcnt vmcnt(8)
	s_waitcnt lgkmcnt(0)
	s_barrier
	v_cmp_eq_f32_e32 vcc, 0, v253
	s_cbranch_vccnz .Lp22sk_1
	s_setprio 1
	s_waitcnt lgkmcnt(0)
	v_mfma_f32_16x16x128_f8f6f4 v[94:97], v[18:25], v[206:213], v[94:97]
	v_mfma_f32_16x16x128_f8f6f4 v[90:93], v[26:33], v[206:213], v[90:93]
	v_mfma_f32_16x16x128_f8f6f4 v[78:81], v[18:25], v[214:221], v[78:81]
	v_mfma_f32_16x16x128_f8f6f4 v[74:77], v[26:33], v[214:221], v[74:77]
	v_mfma_f32_16x16x128_f8f6f4 v[62:65], v[18:25], v[222:229], v[62:65]
	v_mfma_f32_16x16x128_f8f6f4 v[58:61], v[26:33], v[222:229], v[58:61]
	v_mfma_f32_16x16x128_f8f6f4 v[46:49], v[18:25], v[230:237], v[46:49]
	v_mfma_f32_16x16x128_f8f6f4 v[42:45], v[26:33], v[230:237], v[42:45]
	s_nop 7
	s_setprio 0
	s_setprio 1
	v_mfma_f32_16x16x128_f8f6f4 v[86:89], v[2:9], v[206:213], v[86:89]
	v_mfma_f32_16x16x128_f8f6f4 v[82:85], v[10:17], v[206:213], v[82:85]
	v_mfma_f32_16x16x128_f8f6f4 v[70:73], v[2:9], v[214:221], v[70:73]
	v_mfma_f32_16x16x128_f8f6f4 v[66:69], v[10:17], v[214:221], v[66:69]
	v_mfma_f32_16x16x128_f8f6f4 v[54:57], v[2:9], v[222:229], v[54:57]
	v_mfma_f32_16x16x128_f8f6f4 v[50:53], v[10:17], v[222:229], v[50:53]
	v_mfma_f32_16x16x128_f8f6f4 v[38:41], v[2:9], v[230:237], v[38:41]
	v_mfma_f32_16x16x128_f8f6f4 v[34:37], v[10:17], v[230:237], v[34:37]
	s_nop 7
	s_setprio 0
; #define PG8_STAGE(bufoff, gbase, voff) do { _Pragma("unroll") for (int _i = 0; _i < 2; ++_i) \
;         __builtin_amdgcn_global_load_lds((const unsigned*)((const char*)(gbase) + (voff)[_i]), (LAS unsigned*)(lds + (bufoff) + ldsw + _i * 8192), 16, 0, 0); } while (0)
; #define PG8_LDA(dst, b, h) do { _Pragma("unroll") for (int m = 0; m < 4; ++m) dst[m] = PG8_LD8(lds + PG8_SA(b, h) + aoff + m * 2048); } while (0)
; #define PG8_LDB(dst, b, h) do { _Pragma("unroll") for (int n = 0; n < 2; ++n) dst[n] = PG8_LD8(lds + PG8_SB(b, h) + boff + n * 2048); } while (0)
; #define PG8_WAIT_V(n) asm volatile("s_waitcnt vmcnt(" #n ")" ::: "memory")
; #define PG8_WAIT_L(n) asm volatile("s_waitcnt lgkmcnt(" #n ")" ::: "memory")
; #define PG8_BAR __builtin_amdgcn_s_barrier()
; #define PG8_SCHED __builtin_amdgcn_sched_barrier(0)
;     ...
;             PG8_LDB(B0, 1, 0); PG8_LDB(B1, 1, 1); PG8_SCHED; PG8_LDA(At, 1, 0); PG8_STAGE(PG8_SA(0, 1), a2 + hstep, voffA);
;             PG8_WAIT_V(8); PG8_WAIT_L(0); PG8_BAR; PG8_MMA(0, 0, At, B0); PG8_MMA(0, 1, At, B1); PG8_BAR; PG8_SCHED;
;             PG8_LDA(At, 1, 1); PG8_STAGE(PG8_SB(1, 0), b3, voffB); PG8_STAGE(PG8_SB(1, 1), b3 + hstep, voffB); PG8_STAGE(PG8_SA(1, 0), a3, voffA);
;             PG8_WAIT_V(8); PG8_WAIT_L(0); PG8_BAR; PG8_MMA(1, 0, At, B0); PG8_MMA(1, 1, At, B1); PG8_BAR; PG8_SCHED;
.Lp22sk_1:
	s_barrier
	s_add_i32 s72, 0, 0x18000
	s_add_i32 s73, 0, 0x1c000
	v_add_u32_e32 v14, s72, v201
	v_add_u32_e32 v30, s73, v201
	ds_read_b128 v[2:5], v14
	ds_read_b128 v[6:9], v14 offset:1024
	ds_read_b128 v[10:13], v14 offset:2048
	ds_read_b128 v[14:17], v14 offset:3072
	ds_read_b128 v[18:21], v30
	ds_read_b128 v[22:25], v30 offset:1024
	ds_read_b128 v[26:29], v30 offset:2048
	ds_read_b128 v[30:33], v30 offset:3072
	s_add_u32 s70, s70, s22
	s_addc_u32 s71, s71, s23
	s_mov_b32 m0, s35
	v_lshl_add_u64 v[238:239], s[70:71], 0, v[166:167]
	ds_read_b128 v[206:209], v205 offset:32768
	ds_read_b128 v[210:213], v205 offset:33792
	ds_read_b128 v[214:217], v205 offset:34816
	ds_read_b128 v[218:221], v205 offset:35840
	ds_read_b128 v[222:225], v205 offset:36864
	ds_read_b128 v[226:229], v205 offset:37888
	ds_read_b128 v[230:233], v205 offset:38912
	ds_read_b128 v[234:237], v205 offset:39936
	global_load_lds_dwordx4 v[238:239], off
	v_lshl_add_u64 v[238:239], s[70:71], 0, v[168:169]
	s_mov_b32 m0, s44
	s_nop 0
	global_load_lds_dwordx4 v[238:239], off
	s_waitcnt vmcnt(8)
	s_waitcnt lgkmcnt(0)
	s_barrier
	v_cmp_eq_f32_e32 vcc, 0, v252
	s_cbranch_vccnz .Lp22sk_2
	s_setprio 1
	s_waitcnt lgkmcnt(0)
	v_mfma_f32_16x16x128_f8f6f4 v[158:161], v[2:9], v[206:213], v[158:161]
	v_mfma_f32_16x16x128_f8f6f4 v[154:157], v[10:17], v[206:213], v[154:157]
	v_mfma_f32_16x16x128_f8f6f4 v[142:145], v[2:9], v[214:221], v[142:145]
	v_mfma_f32_16x16x128_f8f6f4 v[138:141], v[10:17], v[214:221], v[138:141]
	v_mfma_f32_16x16x128_f8f6f4 v[126:129], v[2:9], v[222:229], v[126:129]
	v_mfma_f32_16x16x128_f8f6f4 v[122:125], v[10:17], v[222:229], v[122:125]
	v_mfma_f32_16x16x128_f8f6f4 v[110:113], v[2:9], v[230:237], v[110:113]
	v_mfma_f32_16x16x128_f8f6f4 v[106:109], v[10:17], v[230:237], v[106:109]
	s_nop 7
	s_setprio 0
	s_setprio 1
	v_mfma_f32_16x16x128_f8f6f4 v[150:153], v[18:25], v[206:213], v[150:153]
	v_mfma_f32_16x16x128_f8f6f4 v[146:149], v[26:33], v[206:213], v[146:149]
	v_mfma_f32_16x16x128_f8f6f4 v[134:137], v[18:25], v[214:221], v[134:137]
	v_mfma_f32_16x16x128_f8f6f4 v[130:133], v[26:33], v[214:221], v[130:133]
	v_mfma_f32_16x16x128_f8f6f4 v[118:121], v[18:25], v[222:229], v[118:121]
	v_mfma_f32_16x16x128_f8f6f4 v[114:117], v[26:33], v[222:229], v[114:117]
	v_mfma_f32_16x16x128_f8f6f4 v[102:105], v[18:25], v[230:237], v[102:105]
	v_mfma_f32_16x16x128_f8f6f4 v[98:101], v[26:33], v[230:237], v[98:101]
	s_nop 7
	s_setprio 0
.Lp22sk_2:
	s_barrier
	s_add_i32 s70, s72, s3
	v_lshl_add_u64 v[176:177], v[176:177], 0, s[28:29]
	s_mov_b32 m0, s70
	ds_read_b128 v[206:209], v205 offset:49152
	ds_read_b128 v[210:213], v205 offset:50176
	ds_read_b128 v[214:217], v205 offset:51200
	ds_read_b128 v[218:221], v205 offset:52224
	ds_read_b128 v[222:225], v205 offset:53248
	ds_read_b128 v[226:229], v205 offset:54272
	ds_read_b128 v[230:233], v205 offset:55296
	ds_read_b128 v[234:237], v205 offset:56320
	global_load_lds_dwordx4 v[176:177], off
	v_lshl_add_u64 v[176:177], v[178:179], 0, s[28:29]
	s_add_i32 m0, s70, 0x2000
	s_add_i32 s70, s73, s3
	global_load_lds_dwordx4 v[176:177], off
	v_lshl_add_u64 v[176:177], v[180:181], 0, s[28:29]
	s_mov_b32 m0, s70
	s_nop 0
	global_load_lds_dwordx4 v[176:177], off
	v_lshl_add_u64 v[176:177], v[182:183], 0, s[28:29]
	s_add_i32 m0, s70, 0x2000
	s_nop 0
	global_load_lds_dwordx4 v[176:177], off
	v_lshl_add_u64 v[176:177], v[184:185], 0, s[28:29]
	s_mov_b32 m0, s50
	s_nop 0
	global_load_lds_dwordx4 v[176:177], off
	v_lshl_add_u64 v[176:177], v[186:187], 0, s[28:29]
	s_mov_b32 m0, s51
	s_nop 0
	global_load_lds_dwordx4 v[176:177], off
	s_waitcnt vmcnt(8)
	s_waitcnt lgkmcnt(0)
	s_barrier
	v_cmp_eq_f32_e32 vcc, 0, v253
	s_cbranch_vccnz .Lp22sk_3
	s_setprio 1
	s_waitcnt lgkmcnt(0)
	v_mfma_f32_16x16x128_f8f6f4 v[94:97], v[2:9], v[206:213], v[94:97]
	v_mfma_f32_16x16x128_f8f6f4 v[90:93], v[10:17], v[206:213], v[90:93]
	v_mfma_f32_16x16x128_f8f6f4 v[78:81], v[2:9], v[214:221], v[78:81]
	v_mfma_f32_16x16x128_f8f6f4 v[74:77], v[10:17], v[214:221], v[74:77]
	v_mfma_f32_16x16x128_f8f6f4 v[62:65], v[2:9], v[222:229], v[62:65]
	v_mfma_f32_16x16x128_f8f6f4 v[58:61], v[10:17], v[222:229], v[58:61]
	v_mfma_f32_16x16x128_f8f6f4 v[46:49], v[2:9], v[230:237], v[46:49]
	v_mfma_f32_16x16x128_f8f6f4 v[42:45], v[10:17], v[230:237], v[42:45]
	s_nop 7
	s_setprio 0
	s_setprio 1
	v_mfma_f32_16x16x128_f8f6f4 v[86:89], v[18:25], v[206:213], v[86:89]
	v_mfma_f32_16x16x128_f8f6f4 v[82:85], v[26:33], v[206:213], v[82:85]
	v_mfma_f32_16x16x128_f8f6f4 v[70:73], v[18:25], v[214:221], v[70:73]
	v_mfma_f32_16x16x128_f8f6f4 v[66:69], v[26:33], v[214:221], v[66:69]
	v_mfma_f32_16x16x128_f8f6f4 v[54:57], v[18:25], v[222:229], v[54:57]
	v_mfma_f32_16x16x128_f8f6f4 v[50:53], v[26:33], v[222:229], v[50:53]
	v_mfma_f32_16x16x128_f8f6f4 v[38:41], v[18:25], v[230:237], v[38:41]
	v_mfma_f32_16x16x128_f8f6f4 v[34:37], v[26:33], v[230:237], v[34:37]
	s_nop 7
	s_setprio 0
.Lp22sk_3:
	s_barrier
	s_add_u32 s68, s68, 0x100
	s_addc_u32 s69, s69, 0
	s_add_u32 s61, s61, 0x100
	s_addc_u32 s80, s80, 0
	s_cmp_ge_i32 s81, s56
	s_mov_b32 s70, s81
	s_cbranch_scc0 .LBB0_2335

; __device__ __forceinline__ u32x4 pack8(f32x4 v0, f32x4 v1) { u32x4 w; w.x = cvt_pk_bf16(v0[0], v0[1]); w.y = cvt_pk_bf16(v0[2], v0[3]); w.z = cvt_pk_bf16(v1[0], v1[1]); w.w = cvt_pk_bf16(v1[2], v1[3]); return w; }
; template <class T> __device__ __forceinline__ void est(T* p, T v) { if constexpr (MK_EPI_NT != 0) __builtin_nontemporal_store(v, p); else *p = v; }
;     __device__ __forceinline__ void operator()(AccT acc, const Unit& u, int wr, int wc, int fr, int fq) const {
;         const int row0 = u.pm * 256 + wr * 64 + fr, col0 = u.pn * 256 + wc * 32 + 8 * fq;
; #pragma unroll
;         for (int ai = 0; ai < 2; ++ai)
; #pragma unroll
;             for (int m = 0; m < 4; ++m) { const int row = row0 + ai * 128 + m * 16; const float g = row_gate[row] * ascale; bf16_t* rp = (u.z == 0 ? YB + (size_t)row * DM : YBX + ((size_t)(u.z - 1) * 2048 + (row - 16384)) * DM) + col0;
; #pragma unroll
;                 for (int bj = 0; bj < 2; ++bj) est((u32x4*)(rp + bj * 128), (u32x4)pack8(acc[ai][bj][m][0] * g, acc[ai][bj][m][1] * g)); }
.LBB0_2338:
	v_lshl_add_u32 v6, s66, 8, v163
	v_ashrrev_i32_e32 v7, 31, v6
	s_nop 15
	s_nop 15
	v_lshl_add_u64 v[2:3], v[6:7], 2, s[6:7]
	global_load_dword v248, v[2:3], off
	global_load_dword v249, v[2:3], off offset:64
	global_load_dword v250, v[2:3], off offset:128
	global_load_dword v251, v[2:3], off offset:192
	v_lshl_or_b32 v4, s79, 8, v202
	v_ashrrev_i32_e32 v5, 31, v4
	v_lshlrev_b64 v[8:9], 12, v[6:7]
	v_lshlrev_b64 v[14:15], 1, v[4:5]
	v_lshl_add_u64 v[4:5], s[14:15], 0, v[8:9]
	v_or_b32_e32 v12, 16, v6
	v_ashrrev_i32_e32 v13, 31, v12
	v_lshl_add_u64 v[4:5], v[4:5], 0, v[14:15]
	v_lshl_add_u64 v[16:17], v[12:13], 2, s[6:7]
	s_waitcnt vmcnt(3)
	v_mov_b32_e32 v10, v248
	global_load_dword v248, v[2:3], off offset:512
	v_mul_f32_e32 v8, 0x3c800000, v10
	v_pk_mul_f32 v[10:11], v[160:161], v[8:9] op_sel_hi:[1,0]
	v_pk_mul_f32 v[18:19], v[158:159], v[8:9] op_sel_hi:[1,0]
	v_pk_mul_f32 v[20:21], v[156:157], v[8:9] op_sel_hi:[1,0]
	v_pk_mul_f32 v[22:23], v[154:155], v[8:9] op_sel_hi:[1,0]
	v_pk_mul_f32 v[24:25], v[152:153], v[8:9] op_sel_hi:[1,0]
	v_pk_mul_f32 v[26:27], v[150:151], v[8:9] op_sel_hi:[1,0]
	v_pk_mul_f32 v[28:29], v[148:149], v[8:9] op_sel_hi:[1,0]
	v_pk_mul_f32 v[30:31], v[146:147], v[8:9] op_sel_hi:[1,0]
	v_cvt_pk_bf16_f32 v8, v18, v19
	v_cvt_pk_bf16_f32 v9, v10, v11
	v_cvt_pk_bf16_f32 v10, v22, v23
	v_cvt_pk_bf16_f32 v11, v20, v21
	global_store_dwordx4 v[4:5], v[8:11], off
	s_nop 1
	v_cvt_pk_bf16_f32 v8, v26, v27
	v_cvt_pk_bf16_f32 v9, v24, v25
	v_cvt_pk_bf16_f32 v10, v30, v31
	v_cvt_pk_bf16_f32 v11, v28, v29
	global_store_dwordx4 v[4:5], v[8:11], off offset:256
	s_nop 0
	v_or_b32_e32 v16, 32, v6
	v_lshlrev_b64 v[8:9], 12, v[12:13]
	v_lshl_add_u64 v[8:9], s[14:15], 0, v[8:9]
	v_lshl_add_u64 v[18:19], v[8:9], 0, v[14:15]
	v_ashrrev_i32_e32 v17, 31, v16
	v_lshl_add_u64 v[12:13], v[16:17], 2, s[6:7]
	s_waitcnt vmcnt(5)
	v_mov_b32_e32 v7, v249
	global_load_dword v249, v[2:3], off offset:576
	v_mul_f32_e32 v8, 0x3c800000, v7
	v_pk_mul_f32 v[10:11], v[144:145], v[8:9] op_sel_hi:[1,0]
	v_pk_mul_f32 v[20:21], v[142:143], v[8:9] op_sel_hi:[1,0]
	v_pk_mul_f32 v[22:23], v[140:141], v[8:9] op_sel_hi:[1,0]
	v_pk_mul_f32 v[24:25], v[138:139], v[8:9] op_sel_hi:[1,0]
	v_pk_mul_f32 v[26:27], v[136:137], v[8:9] op_sel_hi:[1,0]
	v_pk_mul_f32 v[28:29], v[134:135], v[8:9] op_sel_hi:[1,0]
	v_pk_mul_f32 v[30:31], v[132:133], v[8:9] op_sel_hi:[1,0]
	v_pk_mul_f32 v[32:33], v[130:131], v[8:9] op_sel_hi:[1,0]
	v_cvt_pk_bf16_f32 v8, v20, v21
	v_cvt_pk_bf16_f32 v9, v10, v11
	v_cvt_pk_bf16_f32 v10, v24, v25
	v_cvt_pk_bf16_f32 v11, v22, v23
	global_store_dwordx4 v[18:19], v[8:11], off
	s_nop 1
	v_cvt_pk_bf16_f32 v8, v28, v29
	v_cvt_pk_bf16_f32 v9, v26, v27
	v_cvt_pk_bf16_f32 v10, v32, v33
	v_cvt_pk_bf16_f32 v11, v30, v31
	global_store_dwordx4 v[18:19], v[8:11], off offset:256
	s_nop 0
	s_nop 0
	v_or_b32_e32 v10, 48, v6
	v_lshlrev_b64 v[6:7], 12, v[16:17]
	v_lshl_add_u64 v[6:7], s[14:15], 0, v[6:7]
	v_lshl_add_u64 v[16:17], v[6:7], 0, v[14:15]
	v_ashrrev_i32_e32 v11, 31, v10
	v_lshl_add_u64 v[12:13], v[10:11], 2, s[6:7]
	s_waitcnt vmcnt(7)
	v_mov_b32_e32 v8, v250
	global_load_dword v250, v[2:3], off offset:640
	v_mul_f32_e32 v6, 0x3c800000, v8
	v_pk_mul_f32 v[8:9], v[128:129], v[6:7] op_sel_hi:[1,0]
	v_pk_mul_f32 v[18:19], v[126:127], v[6:7] op_sel_hi:[1,0]
	v_pk_mul_f32 v[20:21], v[124:125], v[6:7] op_sel_hi:[1,0]
	v_pk_mul_f32 v[22:23], v[122:123], v[6:7] op_sel_hi:[1,0]
	v_pk_mul_f32 v[24:25], v[120:121], v[6:7] op_sel_hi:[1,0]
	v_pk_mul_f32 v[26:27], v[118:119], v[6:7] op_sel_hi:[1,0]
	v_pk_mul_f32 v[28:29], v[116:117], v[6:7] op_sel_hi:[1,0]
	v_pk_mul_f32 v[30:31], v[114:115], v[6:7] op_sel_hi:[1,0]
	v_cvt_pk_bf16_f32 v6, v18, v19
	v_cvt_pk_bf16_f32 v7, v8, v9
	v_cvt_pk_bf16_f32 v8, v22, v23
	v_cvt_pk_bf16_f32 v9, v20, v21
	global_store_dwordx4 v[16:17], v[6:9], off
	s_nop 1
	v_cvt_pk_bf16_f32 v6, v26, v27
	v_cvt_pk_bf16_f32 v7, v24, v25
	v_cvt_pk_bf16_f32 v8, v30, v31
	v_cvt_pk_bf16_f32 v9, v28, v29
	global_store_dwordx4 v[16:17], v[6:9], off offset:256
	s_nop 0
	s_nop 0
	v_lshlrev_b64 v[6:7], 12, v[10:11]
	v_lshl_add_u64 v[6:7], s[14:15], 0, v[6:7]
	v_lshl_add_u64 v[10:11], v[6:7], 0, v[14:15]
	s_waitcnt vmcnt(9)
; __device__ __forceinline__ u32x4 pack8(f32x4 v0, f32x4 v1) { u32x4 w; w.x = cvt_pk_bf16(v0[0], v0[1]); w.y = cvt_pk_bf16(v0[2], v0[3]); w.z = cvt_pk_bf16(v1[0], v1[1]); w.w = cvt_pk_bf16(v1[2], v1[3]); return w; }
; template <class T> __device__ __forceinline__ void est(T* p, T v) { if constexpr (MK_EPI_NT != 0) __builtin_nontemporal_store(v, p); else *p = v; }
;     __device__ __forceinline__ void operator()(AccT acc, const Unit& u, int wr, int wc, int fr, int fq) const {
;         const int row0 = u.pm * 256 + wr * 64 + fr, col0 = u.pn * 256 + wc * 32 + 8 * fq;
; #pragma unroll
;         for (int ai = 0; ai < 2; ++ai)
; #pragma unroll
;             for (int m = 0; m < 4; ++m) { const int row = row0 + ai * 128 + m * 16; const float g = row_gate[row] * ascale; bf16_t* rp = (u.z == 0 ? YB + (size_t)row * DM : YBX + ((size_t)(u.z - 1) * 2048 + (row - 16384)) * DM) + col0;
; #pragma unroll
;                 for (int bj = 0; bj < 2; ++bj) est((u32x4*)(rp + bj * 128), (u32x4)pack8(acc[ai][bj][m][0] * g, acc[ai][bj][m][1] * g)); }
	v_mov_b32_e32 v8, v251
	global_load_dword v251, v[2:3], off offset:704
	v_mul_f32_e32 v6, 0x3c800000, v8
	v_pk_mul_f32 v[8:9], v[112:113], v[6:7] op_sel_hi:[1,0]
	v_pk_mul_f32 v[12:13], v[110:111], v[6:7] op_sel_hi:[1,0]
	v_pk_mul_f32 v[14:15], v[108:109], v[6:7] op_sel_hi:[1,0]
	v_pk_mul_f32 v[16:17], v[106:107], v[6:7] op_sel_hi:[1,0]
	v_pk_mul_f32 v[18:19], v[104:105], v[6:7] op_sel_hi:[1,0]
	v_pk_mul_f32 v[20:21], v[102:103], v[6:7] op_sel_hi:[1,0]
	v_pk_mul_f32 v[22:23], v[100:101], v[6:7] op_sel_hi:[1,0]
	v_pk_mul_f32 v[24:25], v[98:99], v[6:7] op_sel_hi:[1,0]
	v_cvt_pk_bf16_f32 v6, v12, v13
	v_cvt_pk_bf16_f32 v7, v8, v9
	v_cvt_pk_bf16_f32 v8, v16, v17
	v_cvt_pk_bf16_f32 v9, v14, v15
	global_store_dwordx4 v[10:11], v[6:9], off
	v_add_co_u32_e32 v12, vcc, s74, v4
	s_nop 0
	v_cvt_pk_bf16_f32 v6, v20, v21
	v_cvt_pk_bf16_f32 v7, v18, v19
	v_cvt_pk_bf16_f32 v8, v24, v25
	v_cvt_pk_bf16_f32 v9, v22, v23
	global_store_dwordx4 v[10:11], v[6:9], off offset:256
	s_nop 0
	v_lshl_add_u64 v[10:11], v[4:5], 0, s[38:39]
	v_addc_co_u32_e32 v13, vcc, 0, v5, vcc
	s_waitcnt vmcnt(11)
	v_mov_b32_e32 v6, v248
	v_mul_f32_e32 v6, 0x3c800000, v6
	v_pk_mul_f32 v[8:9], v[96:97], v[6:7] op_sel_hi:[1,0]
	v_pk_mul_f32 v[14:15], v[94:95], v[6:7] op_sel_hi:[1,0]
	v_pk_mul_f32 v[16:17], v[92:93], v[6:7] op_sel_hi:[1,0]
	v_pk_mul_f32 v[18:19], v[90:91], v[6:7] op_sel_hi:[1,0]
	v_pk_mul_f32 v[20:21], v[88:89], v[6:7] op_sel_hi:[1,0]
	v_pk_mul_f32 v[22:23], v[86:87], v[6:7] op_sel_hi:[1,0]
	v_pk_mul_f32 v[24:25], v[84:85], v[6:7] op_sel_hi:[1,0]
	v_pk_mul_f32 v[26:27], v[82:83], v[6:7] op_sel_hi:[1,0]
	v_cvt_pk_bf16_f32 v6, v14, v15
	v_cvt_pk_bf16_f32 v7, v8, v9
	v_cvt_pk_bf16_f32 v8, v18, v19
	v_cvt_pk_bf16_f32 v9, v16, v17
	global_store_dwordx4 v[12:13], v[6:9], off
	v_add_co_u32_e32 v12, vcc, s75, v4
	s_nop 0
	v_cvt_pk_bf16_f32 v6, v22, v23
	v_cvt_pk_bf16_f32 v7, v20, v21
	v_cvt_pk_bf16_f32 v8, v26, v27
	v_cvt_pk_bf16_f32 v9, v24, v25
	global_store_dwordx4 v[10:11], v[6:9], off offset:256
	s_nop 0
	v_lshl_add_u64 v[10:11], v[4:5], 0, s[40:41]
	v_addc_co_u32_e32 v13, vcc, 0, v5, vcc
	s_waitcnt vmcnt(10)
	v_mov_b32_e32 v6, v249
	v_mul_f32_e32 v6, 0x3c800000, v6
	v_pk_mul_f32 v[8:9], v[80:81], v[6:7] op_sel_hi:[1,0]
	v_pk_mul_f32 v[14:15], v[78:79], v[6:7] op_sel_hi:[1,0]
	v_pk_mul_f32 v[16:17], v[76:77], v[6:7] op_sel_hi:[1,0]
	v_pk_mul_f32 v[18:19], v[74:75], v[6:7] op_sel_hi:[1,0]
	v_pk_mul_f32 v[20:21], v[72:73], v[6:7] op_sel_hi:[1,0]
	v_pk_mul_f32 v[22:23], v[70:71], v[6:7] op_sel_hi:[1,0]
	v_pk_mul_f32 v[24:25], v[68:69], v[6:7] op_sel_hi:[1,0]
	v_pk_mul_f32 v[26:27], v[66:67], v[6:7] op_sel_hi:[1,0]
	v_cvt_pk_bf16_f32 v6, v14, v15
	v_cvt_pk_bf16_f32 v7, v8, v9
	v_cvt_pk_bf16_f32 v8, v18, v19
	v_cvt_pk_bf16_f32 v9, v16, v17
	global_store_dwordx4 v[12:13], v[6:9], off
	v_add_co_u32_e32 v12, vcc, s76, v4
	s_nop 0
	v_cvt_pk_bf16_f32 v6, v22, v23
	v_cvt_pk_bf16_f32 v7, v20, v21
	v_cvt_pk_bf16_f32 v8, v26, v27
	v_cvt_pk_bf16_f32 v9, v24, v25
	global_store_dwordx4 v[10:11], v[6:9], off offset:256
	s_nop 0
	v_lshl_add_u64 v[10:11], v[4:5], 0, s[46:47]
	v_addc_co_u32_e32 v13, vcc, 0, v5, vcc
	s_andn2_b64 vcc, exec, s[4:5]
	s_waitcnt vmcnt(9)
	v_mov_b32_e32 v6, v250
	v_mul_f32_e32 v6, 0x3c800000, v6
	v_pk_mul_f32 v[8:9], v[64:65], v[6:7] op_sel_hi:[1,0]
	v_pk_mul_f32 v[14:15], v[62:63], v[6:7] op_sel_hi:[1,0]
	v_pk_mul_f32 v[16:17], v[60:61], v[6:7] op_sel_hi:[1,0]
	v_pk_mul_f32 v[18:19], v[58:59], v[6:7] op_sel_hi:[1,0]
	v_pk_mul_f32 v[20:21], v[56:57], v[6:7] op_sel_hi:[1,0]
	v_pk_mul_f32 v[22:23], v[54:55], v[6:7] op_sel_hi:[1,0]
	v_pk_mul_f32 v[24:25], v[52:53], v[6:7] op_sel_hi:[1,0]
	v_pk_mul_f32 v[26:27], v[50:51], v[6:7] op_sel_hi:[1,0]
	v_cvt_pk_bf16_f32 v6, v14, v15
	v_cvt_pk_bf16_f32 v7, v8, v9
	v_cvt_pk_bf16_f32 v8, v18, v19
	v_cvt_pk_bf16_f32 v9, v16, v17
	global_store_dwordx4 v[12:13], v[6:9], off
	s_nop 1
	v_cvt_pk_bf16_f32 v6, v22, v23
	v_cvt_pk_bf16_f32 v7, v20, v21
	v_cvt_pk_bf16_f32 v8, v26, v27
	v_cvt_pk_bf16_f32 v9, v24, v25
	global_store_dwordx4 v[10:11], v[6:9], off offset:256
	s_nop 0
	s_waitcnt vmcnt(8)
	v_mov_b32_e32 v2, v251
	v_mul_f32_e32 v2, 0x3c800000, v2
	v_add_co_u32_e64 v8, s[4:5], s77, v4
	v_lshl_add_u64 v[6:7], v[4:5], 0, s[48:49]
	s_nop 0
	v_addc_co_u32_e64 v9, s[4:5], 0, v5, s[4:5]
	v_pk_mul_f32 v[4:5], v[48:49], v[2:3] op_sel_hi:[1,0]
	v_pk_mul_f32 v[10:11], v[46:47], v[2:3] op_sel_hi:[1,0]
	v_pk_mul_f32 v[12:13], v[44:45], v[2:3] op_sel_hi:[1,0]
	v_pk_mul_f32 v[14:15], v[42:43], v[2:3] op_sel_hi:[1,0]
	v_pk_mul_f32 v[16:17], v[40:41], v[2:3] op_sel_hi:[1,0]
	v_pk_mul_f32 v[18:19], v[38:39], v[2:3] op_sel_hi:[1,0]
	v_pk_mul_f32 v[20:21], v[36:37], v[2:3] op_sel_hi:[1,0]
	v_pk_mul_f32 v[22:23], v[34:35], v[2:3] op_sel_hi:[1,0]
	v_cvt_pk_bf16_f32 v2, v10, v11
	v_cvt_pk_bf16_f32 v3, v4, v5
	v_cvt_pk_bf16_f32 v4, v14, v15
	v_cvt_pk_bf16_f32 v5, v12, v13
	s_mov_b64 s[4:5], -1
	global_store_dwordx4 v[8:9], v[2:5], off
	s_nop 1
	v_cvt_pk_bf16_f32 v2, v18, v19
	v_cvt_pk_bf16_f32 v3, v16, v17
	v_cvt_pk_bf16_f32 v4, v22, v23
	v_cvt_pk_bf16_f32 v5, v20, v21
	global_store_dwordx4 v[6:7], v[2:5], off offset:256
	s_cbranch_vccnz .LBB0_2326
	s_andn2_b64 vcc, exec, s[24:25]
	s_cbranch_vccnz .LBB0_2325
	s_barrier
	s_branch .LBB0_2325
